# baseline (speedup 1.0000x reference)
_Z6k_gemmILi4EEvPKtS1_PvPKfS4_S4_ii:
	s_load_dwordx2 s[8:9], s[0:1], 0x30
	s_load_dwordx4 s[4:7], s[0:1], 0x0
	s_waitcnt lgkmcnt(0)
	s_and_b32 s26, s2, 7
	s_lshl_b32 s26, s26, 5
	s_lshr_b32 s3, s2, 3
	s_add_i32 s26, s26, s3
	s_mov_b32 s27, 0
	s_mov_b32 s28, 0
	s_mov_b32 s29, 0
	s_lshr_b32 s33, s26, 2
	s_lshl_b32 s30, s33, 2
	s_and_b32 s3, s26, 3
	v_lshlrev_b32_e32 v2, 4, v0
	v_and_b32_e32 v3, 32, v0
	v_bfe_u32 v4, v0, 2, 4
	v_bitop3_b32 v2, v2, v3, 48 bitop3:0x6c
	v_mov_b32_e32 v131, 0
	s_mov_b64 s[18:19], 0x400
	s_mov_b64 s[24:25], 0x10000
	s_lshl_b32 s2, s33, 2
	s_and_b32 s16, s2, 0xffffffc0
	s_ashr_i32 s17, s16, 31
	s_lshl_b32 s2, s33, 12
	s_lshl_b32 s8, s3, 8
	s_lshl_b64 s[12:13], s[16:17], 16
	s_and_b32 s17, s2, 0xf000
	s_add_u32 s2, s6, s12
	s_addc_u32 s3, s7, s13
	v_lshrrev_b32_e32 v1, 3, v0
	v_readfirstlane_b32 s9, v0
	s_add_u32 s2, s2, s17
	v_and_or_b32 v1, v1, 48, v4
	s_addc_u32 s3, s3, 0
	s_lshl_b32 s9, s9, 4
	v_and_or_b32 v4, v0, 64, v2
	v_lshlrev_b32_e32 v2, 4, v1
	s_and_b32 s31, s9, 0x7ffffc00
	v_lshl_or_b32 v140, v4, 12, v2
	s_add_i32 s43, s31, 0
	s_add_i32 s44, s43, 0x10000
	v_mov_b32_e32 v2, v140
	s_mov_b32 m0, s44
	v_mov_b32_e32 v130, v140
	global_load_lds_dwordx4 v2, s[2:3] sc0
	s_add_i32 s45, s43, 0x12000
	v_lshl_add_u64 v[2:3], s[2:3], 0, v[130:131]
	s_ashr_i32 s9, s8, 31
	v_lshl_add_u64 v[2:3], v[2:3], 0, s[18:19]
	s_mov_b32 m0, s45
	v_lshl_or_b32 v1, v1, 10, v4
	s_lshl_b64 s[10:11], s[8:9], 10
	global_load_lds_dwordx4 v[2:3], off sc0
	s_add_u32 s14, s4, s10
	v_mov_b32_e32 v2, v1
	s_addc_u32 s15, s5, s11
	s_mov_b32 m0, s43
	v_mov_b32_e32 v130, v1
	global_load_lds_dwordx4 v2, s[14:15]
	s_add_i32 s46, s43, 0x2000
	v_lshl_add_u64 v[2:3], s[14:15], 0, v[130:131]
	v_lshl_add_u64 v[2:3], v[2:3], 0, s[24:25]
	s_mov_b32 m0, s46
	v_mov_b32_e32 v130, v140
	global_load_lds_dwordx4 v[2:3], off
	s_add_i32 s47, s43, 0x14000
	s_mov_b64 s[20:21], 0x800
	v_lshl_add_u64 v[2:3], s[2:3], 0, v[130:131]
	v_lshl_add_u64 v[2:3], v[2:3], 0, s[20:21]
	s_mov_b32 m0, s47
	v_mov_b32_e32 v130, v140
	global_load_lds_dwordx4 v[2:3], off sc0
	s_mov_b64 s[22:23], 0xc00
	v_lshl_add_u64 v[2:3], s[2:3], 0, v[130:131]
	s_or_b32 s2, s8, 0x80
	s_ashr_i32 s3, s2, 31
	s_add_i32 s48, s43, 0x16000
	s_lshl_b64 s[2:3], s[2:3], 10
	v_lshl_add_u64 v[2:3], v[2:3], 0, s[22:23]
	s_mov_b32 m0, s48
	s_add_u32 s10, s4, s2
	global_load_lds_dwordx4 v[2:3], off sc0
	s_addc_u32 s11, s5, s3
	s_add_i32 s49, s43, 0x4000
	v_mov_b32_e32 v2, v1
	s_mov_b32 m0, s49
	v_mov_b32_e32 v130, v1
	global_load_lds_dwordx4 v2, s[10:11]
	s_add_i32 s50, s43, 0x6000
	v_lshl_add_u64 v[2:3], s[10:11], 0, v[130:131]
	v_lshl_add_u64 v[2:3], v[2:3], 0, s[24:25]
	s_mov_b32 m0, s50
	s_load_dwordx4 s[0:3], s[0:1], 0x10
	global_load_lds_dwordx4 v[2:3], off
	v_lshrrev_b32_e32 v2, 8, v0
	v_cmp_eq_u32_e32 vcc, 1, v2
	s_and_saveexec_b64 s[24:25], vcc
	s_cbranch_execz .LBB3_6
	s_barrier
